# P11 combine loop: next token's routing index loads prefetched one iteration ahead so the expert-row loads issue without waiting for a first round trip
# baseline (speedup 1.0000x reference)
; #define GAS __attribute__((address_space(1)))
; __device__ __forceinline__ void p11_combine(const P& p, int gw, int NGW, int lane, float oscale) {
;     const int* cnt = (const int*)(p.ws + WS_CTL) + CW_CNT; const unsigned char* Y = (const unsigned char*)(p.ws + WS_Y);
;     const int* tope = (const int*)(p.ws + WS_TOPE); const float* topg = (const float*)(p.ws + WS_TOPG); const int* tpos = (const int*)(p.ws + WS_TPOS);
;     int pad = lane < NE ? ((cnt[lane & 31] + 255) >> 8) : 0; int inc = pad;
; #pragma unroll
;     for (int o = 1; o < 32; o <<= 1) { const int t = __shfl_up(inc, o); if ((lane & 31) >= o) inc += t; }
;     const int toff_l = inc - pad;
;     for (int m = gw; m < NTOK; m += NGW) {
;         GAS f32x4* xr = (GAS f32x4*)(p.out + (size_t)m * DM) + lane;
;         const GAS v2u* x2r = (const GAS v2u*)((const bf16*)(p.ws + WS_X2H) + (size_t)m * DM) + lane;
;         f32x4 a[8];
; #pragma unroll
;         for (int j = 0; j < 8; ++j) { const v2u w = x2r[64 * j]; a[j] = (f32x4){__uint_as_float(w.x << 16), __uint_as_float(w.x & 0xffff0000u), __uint_as_float(w.y << 16), __uint_as_float(w.y & 0xffff0000u)}; }
; #pragma unroll
;         for (int k = 0; k < TOPK; ++k) { const int e = tope[m * 4 + k]; const float g = topg[m * 4 + k]; const int slot = 256 * __shfl(toff_l, e) + tpos[m * 4 + k];
.LBB5_1740:
	s_or_b64 exec, exec, s[0:1]
	v_mbcnt_lo_u32_b32 v1, -1, 0
	v_mbcnt_hi_u32_b32 v1, -1, v1
	v_and_b32_e32 v38, 64, v1
	v_add_u32_e32 v3, -1, v1
	v_cmp_lt_i32_e32 vcc, v3, v38
	v_and_b32_e32 v0, 31, v0
	s_waitcnt lgkmcnt(0)
	v_add_u32_e32 v4, -2, v1
	v_cndmask_b32_e32 v3, v3, v1, vcc
	v_lshlrev_b32_e32 v3, 2, v3
	ds_bpermute_b32 v3, v3, v2
	v_cmp_ne_u32_e32 vcc, 0, v0
	s_cmpk_gt_i32 s28, 0x7fff
	s_waitcnt lgkmcnt(0)
	v_cndmask_b32_e32 v3, 0, v3, vcc
	v_cmp_lt_i32_e32 vcc, v4, v38
	v_add_u32_e32 v3, v3, v2
	s_nop 0
	v_cndmask_b32_e32 v4, v4, v1, vcc
	v_lshlrev_b32_e32 v4, 2, v4
	ds_bpermute_b32 v4, v4, v3
	v_cmp_lt_u32_e32 vcc, 1, v0
	s_waitcnt lgkmcnt(0)
	s_nop 0
	v_cndmask_b32_e32 v4, 0, v4, vcc
	v_add_u32_e32 v3, v4, v3
	v_add_u32_e32 v4, -4, v1
	v_cmp_lt_i32_e32 vcc, v4, v38
	s_nop 1
	v_cndmask_b32_e32 v4, v4, v1, vcc
	v_lshlrev_b32_e32 v4, 2, v4
	ds_bpermute_b32 v4, v4, v3
	v_cmp_lt_u32_e32 vcc, 3, v0
	s_waitcnt lgkmcnt(0)
	s_nop 0
	v_cndmask_b32_e32 v4, 0, v4, vcc
	v_add_u32_e32 v3, v4, v3
	v_add_u32_e32 v4, -8, v1
	v_cmp_lt_i32_e32 vcc, v4, v38
	s_nop 1
	v_cndmask_b32_e32 v4, v4, v1, vcc
	v_lshlrev_b32_e32 v4, 2, v4
	ds_bpermute_b32 v4, v4, v3
	v_cmp_lt_u32_e32 vcc, 7, v0
	s_waitcnt lgkmcnt(0)
	s_nop 0
	v_cndmask_b32_e32 v4, 0, v4, vcc
	v_add_u32_e32 v3, v4, v3
	v_add_u32_e32 v4, -16, v1
	v_cmp_lt_i32_e32 vcc, v4, v38
	s_nop 1
	v_cndmask_b32_e32 v4, v4, v1, vcc
	v_lshlrev_b32_e32 v4, 2, v4
	ds_bpermute_b32 v4, v4, v3
	s_cbranch_scc1 .LBB5_1743
	v_cmp_lt_u32_e32 vcc, 15, v0
	v_sub_u32_e32 v2, v3, v2
	v_readlane_b32 s12, v253, 2
	s_waitcnt lgkmcnt(0)
	v_cndmask_b32_e32 v0, 0, v4, vcc
	v_add_u32_e32 v39, v2, v0
	v_add_u32_e32 v0, 64, v38
	v_xor_b32_e32 v2, 1, v1
	v_cmp_lt_i32_e32 vcc, v2, v0
	s_add_u32 s6, s22, 0x3100000
	v_lshlrev_b32_e32 v4, 4, v198
	v_cndmask_b32_e32 v2, v1, v2, vcc
	v_lshlrev_b32_e32 v40, 2, v2
	v_xor_b32_e32 v2, 2, v1
	v_cmp_lt_i32_e32 vcc, v2, v0
	v_mov_b32_e32 v5, 0
	v_readlane_b32 s18, v253, 8
	v_cndmask_b32_e32 v2, v1, v2, vcc
	v_lshlrev_b32_e32 v41, 2, v2
	v_xor_b32_e32 v2, 4, v1
	v_cmp_lt_i32_e32 vcc, v2, v0
	v_readlane_b32 s19, v253, 9
	s_addc_u32 s7, s23, 0
	v_cndmask_b32_e32 v2, v1, v2, vcc
	v_lshlrev_b32_e32 v42, 2, v2
	v_xor_b32_e32 v2, 8, v1
	v_cmp_lt_i32_e32 vcc, v2, v0
	v_lshl_add_u64 v[6:7], s[18:19], 0, v[4:5]
	s_mov_b64 s[0:1], 0x1400
	v_cndmask_b32_e32 v2, v1, v2, vcc
	v_lshlrev_b32_e32 v43, 2, v2
	v_xor_b32_e32 v2, 16, v1
	v_cmp_lt_i32_e32 vcc, v2, v0
	s_add_u32 s8, s22, 0x3180000
	v_lshl_add_u64 v[10:11], v[6:7], 0, s[0:1]
	v_cndmask_b32_e32 v2, v1, v2, vcc
	v_lshlrev_b32_e32 v44, 2, v2
	v_xor_b32_e32 v2, 32, v1
	v_cmp_lt_i32_e32 vcc, v2, v0
	s_mov_b64 s[0:1], 0x1800
	s_addc_u32 s9, s23, 0
	v_cndmask_b32_e32 v0, v1, v2, vcc
	v_lshlrev_b32_e32 v45, 2, v0
	v_lshl_add_u64 v[12:13], v[6:7], 0, s[0:1]
	s_mov_b64 s[0:1], 0x1c00
	v_lshlrev_b32_e32 v0, 2, v198
	v_mov_b32_e32 v1, v5
	s_add_u32 s10, s22, 0x3200000
	v_lshl_add_u64 v[14:15], v[6:7], 0, s[0:1]
	v_lshl_add_u64 v[0:1], s[22:23], 0, v[0:1]
	s_mov_b64 s[0:1], 0x8a000000
	s_addc_u32 s11, s23, 0
	v_lshl_add_u64 v[16:17], v[0:1], 0, s[0:1]
	s_lshl_b32 s0, s94, 5
	s_lshl_b32 s1, s95, 2
	s_ashr_i32 s29, s28, 31
	s_add_i32 s0, s0, s1
	s_lshl_b32 s12, s33, 5
	s_lshl_b64 s[4:5], s[28:29], 13
	s_add_u32 s4, s20, s4
	s_addc_u32 s5, s21, s5
	s_mov_b64 s[2:3], 0x1000
	v_lshl_add_u64 v[0:1], s[4:5], 0, v[4:5]
	s_ashr_i32 s27, s26, 31
	v_lshl_add_u64 v[8:9], v[6:7], 0, s[2:3]
	v_lshl_add_u64 v[18:19], v[0:1], 0, s[2:3]
	s_lshl_b64 s[2:3], s[26:27], 13
	s_lshl_b64 s[4:5], s[28:29], 12
	s_add_u32 s4, s22, s4
	v_lshlrev_b32_e32 v4, 3, v198
	s_addc_u32 s5, s23, s5
	v_readlane_b32 s13, v253, 3
	v_lshl_add_u64 v[0:1], s[4:5], 0, v[4:5]
	s_mov_b64 s[4:5], 0xac000000
	v_lshl_add_u64 v[20:21], v[0:1], 0, s[4:5]
	s_lshl_b64 s[4:5], s[26:27], 12
	v_mov_b32_e32 v4, 0x358637bd
	s_mov_b32 s13, 0x800000
	v_readlane_b32 s14, v253, 4
	v_readlane_b32 s15, v253, 5
	v_readlane_b32 s16, v253, 6
	v_readlane_b32 s17, v253, 7
	s_ashr_i32 s1, s0, 31
	s_lshl_b64 s[14:15], s[0:1], 2
	s_add_u32 s16, s6, s14
	s_addc_u32 s17, s7, s15
	global_load_dwordx4 v[200:203], v5, s[16:17]
	s_add_u32 s16, s8, s14
	s_addc_u32 s17, s9, s15
	s_add_u32 s14, s10, s14
	s_addc_u32 s15, s11, s15
	global_load_dword v204, v5, s[16:17]
	global_load_dword v205, v5, s[14:15]
	s_add_i32 s16, s0, 1
	s_ashr_i32 s17, s16, 31
	s_lshl_b64 s[14:15], s[16:17], 2
	s_add_u32 s16, s8, s14
	s_addc_u32 s17, s9, s15
	s_add_u32 s14, s10, s14
	s_addc_u32 s15, s11, s15
	global_load_dwordx3 v[206:208], v5, s[16:17]
	global_load_dword v209, v5, s[14:15]
	s_add_i32 s16, s0, 2
	s_ashr_i32 s17, s16, 31
	s_lshl_b64 s[14:15], s[16:17], 2
	s_add_u32 s14, s10, s14
	s_addc_u32 s15, s11, s15
	global_load_dwordx2 v[210:211], v5, s[14:15]
	global_load_dwordx4 v[164:167], v[6:7], off offset:1024
	global_load_dwordx4 v[168:171], v[6:7], off offset:2048
	global_load_dwordx4 v[172:175], v[6:7], off offset:3072
	global_load_dwordx4 v[176:179], v[8:9], off
	global_load_dwordx4 v[180:183], v[10:11], off
	global_load_dwordx4 v[184:187], v[12:13], off
	global_load_dwordx4 v[188:191], v[14:15], off
	s_waitcnt vmcnt(0)
; #define GAS __attribute__((address_space(1)))
; __device__ __forceinline__ void p11_combine(const P& p, int gw, int NGW, int lane, float oscale) {
;     ...
;     for (int m = gw; m < NTOK; m += NGW) {
;         GAS f32x4* xr = (GAS f32x4*)(p.out + (size_t)m * DM) + lane;
;         const GAS v2u* x2r = (const GAS v2u*)((const bf16*)(p.ws + WS_X2H) + (size_t)m * DM) + lane;
;         f32x4 a[8];
; #pragma unroll
;         for (int j = 0; j < 8; ++j) { const v2u w = x2r[64 * j]; a[j] = (f32x4){__uint_as_float(w.x << 16), __uint_as_float(w.x & 0xffff0000u), __uint_as_float(w.y << 16), __uint_as_float(w.y & 0xffff0000u)}; }
; #pragma unroll
;         for (int k = 0; k < TOPK; ++k) { const int e = tope[m * 4 + k]; const float g = topg[m * 4 + k]; const int slot = 256 * __shfl(toff_l, e) + tpos[m * 4 + k];
;             const GAS unsigned* yr = (const GAS unsigned*)(Y + (size_t)slot * DM) + lane;
; #pragma unroll
;             for (int j = 0; j < 8; ++j) { const int w = (int)yr[64 * j]; const f32x2 lo = __builtin_amdgcn_cvt_pk_f32_fp8(w, false), hi = __builtin_amdgcn_cvt_pk_f32_fp8(w, true);
;                 a[j].x += g * lo.x; a[j].y += g * lo.y; a[j].z += g * hi.x; a[j].w += g * hi.y; } }
.LBB5_1742:
	v_mov_b32_e32 v46, v200
	v_mov_b32_e32 v47, v201
	v_mov_b32_e32 v48, v202
	v_mov_b32_e32 v49, v203
	v_mov_b32_e32 v54, v204
	v_mov_b32_e32 v53, v205
	v_mov_b32_e32 v50, v206
	v_mov_b32_e32 v51, v207
	v_mov_b32_e32 v52, v208
	v_mov_b32_e32 v55, v209
	v_mov_b32_e32 v56, v210
	v_mov_b32_e32 v57, v211
	global_load_dwordx2 v[36:37], v[20:21], off
	global_load_dwordx2 v[34:35], v[20:21], off offset:512
	global_load_dwordx2 v[32:33], v[20:21], off offset:1024
	global_load_dwordx2 v[30:31], v[20:21], off offset:1536
	global_load_dwordx2 v[28:29], v[20:21], off offset:2048
	global_load_dwordx2 v[26:27], v[20:21], off offset:2560
	global_load_dwordx2 v[24:25], v[20:21], off offset:3072
	global_load_dwordx2 v[22:23], v[20:21], off offset:3584
	global_load_dwordx4 v[0:3], v[6:7], off
	s_add_i32 s28, s28, s26
	s_add_i32 s0, s0, s12
	v_lshl_add_u64 v[20:21], v[20:21], 0, s[4:5]
	s_ashr_i32 s1, s0, 31
	s_lshl_b64 s[14:15], s[0:1], 2
	s_add_u32 s16, s6, s14
	s_addc_u32 s17, s7, s15
	global_load_dwordx4 v[200:203], v5, s[16:17]
	s_add_u32 s16, s8, s14
	s_addc_u32 s17, s9, s15
	s_add_u32 s14, s10, s14
	s_addc_u32 s15, s11, s15
	global_load_dword v204, v5, s[16:17]
	global_load_dword v205, v5, s[14:15]
	s_add_i32 s16, s0, 1
	s_ashr_i32 s17, s16, 31
	s_lshl_b64 s[14:15], s[16:17], 2
	s_add_u32 s16, s8, s14
	s_addc_u32 s17, s9, s15
	s_add_u32 s14, s10, s14
	s_addc_u32 s15, s11, s15
	global_load_dwordx3 v[206:208], v5, s[16:17]
	global_load_dword v209, v5, s[14:15]
	s_add_i32 s16, s0, 2
	s_ashr_i32 s17, s16, 31
	s_lshl_b64 s[14:15], s[16:17], 2
	s_add_u32 s14, s10, s14
	s_addc_u32 s15, s11, s15
	global_load_dwordx2 v[210:211], v5, s[14:15]
	s_cmp_lt_i32 s28, 0x8000
	v_and_or_b32 v46, v46, 63, v38
	v_lshlrev_b32_e32 v46, 2, v46
	v_and_or_b32 v47, v47, 63, v38
	ds_bpermute_b32 v46, v46, v39
	v_lshlrev_b32_e32 v47, 2, v47
	ds_bpermute_b32 v74, v47, v39
	v_and_or_b32 v48, v48, 63, v38
	v_and_or_b32 v49, v49, 63, v38
	v_lshlrev_b32_e32 v48, 2, v48
	s_waitcnt lgkmcnt(1)
	v_lshl_add_u32 v46, v46, 8, v53
	v_lshlrev_b32_e32 v49, 2, v49
	ds_bpermute_b32 v75, v48, v39
	v_ashrrev_i32_e32 v47, 31, v46
	ds_bpermute_b32 v49, v49, v39
	v_mov_b32_e32 v48, v52
	v_lshlrev_b64 v[46:47], 11, v[46:47]
	s_waitcnt lgkmcnt(2)
	v_lshl_add_u32 v52, v74, 8, v55
	v_lshl_add_u64 v[46:47], v[16:17], 0, v[46:47]
	v_ashrrev_i32_e32 v53, 31, v52
	global_load_dword v55, v[46:47], off
	global_load_dword v74, v[46:47], off offset:256
	global_load_dword v78, v[46:47], off offset:512
	global_load_dword v82, v[46:47], off offset:768
	global_load_dword v86, v[46:47], off offset:1024
	global_load_dword v90, v[46:47], off offset:1280
	global_load_dword v94, v[46:47], off offset:1536
	global_load_dword v98, v[46:47], off offset:1792
	v_lshlrev_b64 v[46:47], 11, v[52:53]
	v_lshl_add_u64 v[46:47], v[16:17], 0, v[46:47]
	global_load_dword v102, v[46:47], off
	global_load_dword v106, v[46:47], off offset:256
	global_load_dword v110, v[46:47], off offset:512
	global_load_dword v114, v[46:47], off offset:768
	global_load_dword v118, v[46:47], off offset:1024
	global_load_dword v122, v[46:47], off offset:1280
	global_load_dword v126, v[46:47], off offset:1536
	global_load_dword v130, v[46:47], off offset:1792
	s_waitcnt lgkmcnt(1)
	v_lshl_add_u32 v46, v75, 8, v56
	s_waitcnt lgkmcnt(0)
	v_lshl_add_u32 v52, v49, 8, v57
	v_ashrrev_i32_e32 v47, 31, v46
	v_ashrrev_i32_e32 v53, 31, v52
	v_lshlrev_b64 v[46:47], 11, v[46:47]
	v_lshlrev_b64 v[52:53], 11, v[52:53]
	v_lshl_add_u64 v[46:47], v[16:17], 0, v[46:47]
	v_lshl_add_u64 v[52:53], v[16:17], 0, v[52:53]
	global_load_dword v49, v[46:47], off
	global_load_dword v132, v[46:47], off offset:256
	global_load_dword v133, v[46:47], off offset:512
	global_load_dword v134, v[46:47], off offset:768
	global_load_dword v135, v[46:47], off offset:1024
	global_load_dword v136, v[46:47], off offset:1280
	global_load_dword v137, v[46:47], off offset:1536
	global_load_dword v138, v[46:47], off offset:1792
	global_load_dword v139, v[52:53], off
	global_load_dword v140, v[52:53], off offset:256
	global_load_dword v141, v[52:53], off offset:512
	global_load_dword v142, v[52:53], off offset:768
	global_load_dword v143, v[52:53], off offset:1024
	global_load_dword v144, v[52:53], off offset:1280
	global_load_dword v145, v[52:53], off offset:1536
	global_load_dword v146, v[52:53], off offset:1792
	s_waitcnt vmcnt(39)
	v_lshlrev_b32_e32 v58, 16, v36
	v_and_b32_e32 v59, 0xffff0000, v36
	v_lshlrev_b32_e32 v36, 16, v37
	v_and_b32_e32 v37, 0xffff0000, v37
	v_lshlrev_b32_e32 v60, 16, v34
	v_and_b32_e32 v61, 0xffff0000, v34
	v_lshlrev_b32_e32 v34, 16, v35
	v_and_b32_e32 v35, 0xffff0000, v35
	v_lshlrev_b32_e32 v62, 16, v32
	v_and_b32_e32 v63, 0xffff0000, v32
	v_lshlrev_b32_e32 v32, 16, v33
	v_and_b32_e32 v33, 0xffff0000, v33
	v_lshlrev_b32_e32 v64, 16, v30
	v_and_b32_e32 v65, 0xffff0000, v30
	v_lshlrev_b32_e32 v30, 16, v31
	v_and_b32_e32 v31, 0xffff0000, v31
	v_lshlrev_b32_e32 v66, 16, v28
	v_and_b32_e32 v67, 0xffff0000, v28
	v_lshlrev_b32_e32 v28, 16, v29
	v_and_b32_e32 v29, 0xffff0000, v29
	v_lshlrev_b32_e32 v68, 16, v26
	v_and_b32_e32 v69, 0xffff0000, v26
	v_lshlrev_b32_e32 v26, 16, v27
	v_and_b32_e32 v27, 0xffff0000, v27
	v_lshlrev_b32_e32 v70, 16, v24
	v_and_b32_e32 v71, 0xffff0000, v24
	v_lshlrev_b32_e32 v24, 16, v25
	v_and_b32_e32 v25, 0xffff0000, v25
	v_lshlrev_b32_e32 v72, 16, v22
	v_and_b32_e32 v73, 0xffff0000, v22
	v_lshlrev_b32_e32 v22, 16, v23
	v_and_b32_e32 v23, 0xffff0000, v23
	s_waitcnt vmcnt(31)
	v_cvt_pk_f32_fp8_e32 v[46:47], v55
	v_cvt_pk_f32_fp8_sdwa v[52:53], v55 src0_sel:WORD_1
	s_waitcnt vmcnt(30)
	v_cvt_pk_f32_fp8_e32 v[56:57], v74
	v_cvt_pk_f32_fp8_sdwa v[74:75], v74 src0_sel:WORD_1
	s_waitcnt vmcnt(29)
; #define GAS __attribute__((address_space(1)))
; __device__ __forceinline__ void p11_combine(const P& p, int gw, int NGW, int lane, float oscale) {
;     ...
;         for (int k = 0; k < TOPK; ++k) { const int e = tope[m * 4 + k]; const float g = topg[m * 4 + k]; const int slot = 256 * __shfl(toff_l, e) + tpos[m * 4 + k];
;             const GAS unsigned* yr = (const GAS unsigned*)(Y + (size_t)slot * DM) + lane;
; #pragma unroll
;             for (int j = 0; j < 8; ++j) { const int w = (int)yr[64 * j]; const f32x2 lo = __builtin_amdgcn_cvt_pk_f32_fp8(w, false), hi = __builtin_amdgcn_cvt_pk_f32_fp8(w, true);
;                 a[j].x += g * lo.x; a[j].y += g * lo.y; a[j].z += g * hi.x; a[j].w += g * hi.y; } }
	v_cvt_pk_f32_fp8_e32 v[76:77], v78
	v_cvt_pk_f32_fp8_sdwa v[78:79], v78 src0_sel:WORD_1
	s_waitcnt vmcnt(28)
	v_cvt_pk_f32_fp8_e32 v[80:81], v82
	v_cvt_pk_f32_fp8_sdwa v[82:83], v82 src0_sel:WORD_1
	s_waitcnt vmcnt(27)
	v_cvt_pk_f32_fp8_e32 v[84:85], v86
	v_cvt_pk_f32_fp8_sdwa v[86:87], v86 src0_sel:WORD_1
	s_waitcnt vmcnt(26)
	v_cvt_pk_f32_fp8_e32 v[88:89], v90
	v_cvt_pk_f32_fp8_sdwa v[90:91], v90 src0_sel:WORD_1
	s_waitcnt vmcnt(25)
	v_cvt_pk_f32_fp8_e32 v[92:93], v94
	v_cvt_pk_f32_fp8_sdwa v[94:95], v94 src0_sel:WORD_1
	s_waitcnt vmcnt(24)
	v_cvt_pk_f32_fp8_e32 v[96:97], v98
	v_cvt_pk_f32_fp8_sdwa v[98:99], v98 src0_sel:WORD_1
	s_waitcnt vmcnt(23)
	v_cvt_pk_f32_fp8_e32 v[100:101], v102
	v_cvt_pk_f32_fp8_sdwa v[102:103], v102 src0_sel:WORD_1
	s_waitcnt vmcnt(22)
	v_cvt_pk_f32_fp8_e32 v[104:105], v106
	v_cvt_pk_f32_fp8_sdwa v[106:107], v106 src0_sel:WORD_1
	s_waitcnt vmcnt(21)
	v_cvt_pk_f32_fp8_e32 v[108:109], v110
	s_waitcnt vmcnt(20)
	v_cvt_pk_f32_fp8_e32 v[112:113], v114
	s_waitcnt vmcnt(19)
	v_cvt_pk_f32_fp8_e32 v[116:117], v118
	s_waitcnt vmcnt(18)
	v_cvt_pk_f32_fp8_e32 v[120:121], v122
	s_waitcnt vmcnt(17)
	v_cvt_pk_f32_fp8_e32 v[124:125], v126
	v_cvt_pk_f32_fp8_sdwa v[110:111], v110 src0_sel:WORD_1
	v_cvt_pk_f32_fp8_sdwa v[114:115], v114 src0_sel:WORD_1
	v_cvt_pk_f32_fp8_sdwa v[118:119], v118 src0_sel:WORD_1
	v_cvt_pk_f32_fp8_sdwa v[122:123], v122 src0_sel:WORD_1
	v_cvt_pk_f32_fp8_sdwa v[126:127], v126 src0_sel:WORD_1
	s_waitcnt vmcnt(16)
	v_cvt_pk_f32_fp8_e32 v[128:129], v130
	v_cvt_pk_f32_fp8_sdwa v[130:131], v130 src0_sel:WORD_1
	v_pk_fma_f32 v[46:47], v[54:55], v[46:47], v[58:59] op_sel_hi:[0,1,1]
	v_pk_fma_f32 v[36:37], v[54:55], v[52:53], v[36:37] op_sel_hi:[0,1,1]
	v_pk_fma_f32 v[52:53], v[54:55], v[56:57], v[60:61] op_sel_hi:[0,1,1]
	v_pk_fma_f32 v[34:35], v[54:55], v[74:75], v[34:35] op_sel_hi:[0,1,1]
	v_pk_fma_f32 v[56:57], v[54:55], v[76:77], v[62:63] op_sel_hi:[0,1,1]
	v_pk_fma_f32 v[32:33], v[54:55], v[78:79], v[32:33] op_sel_hi:[0,1,1]
	v_pk_fma_f32 v[58:59], v[54:55], v[80:81], v[64:65] op_sel_hi:[0,1,1]
	v_pk_fma_f32 v[30:31], v[54:55], v[82:83], v[30:31] op_sel_hi:[0,1,1]
	v_pk_fma_f32 v[60:61], v[54:55], v[84:85], v[66:67] op_sel_hi:[0,1,1]
	v_pk_fma_f32 v[28:29], v[54:55], v[86:87], v[28:29] op_sel_hi:[0,1,1]
	v_pk_fma_f32 v[62:63], v[54:55], v[88:89], v[68:69] op_sel_hi:[0,1,1]
	v_pk_fma_f32 v[26:27], v[54:55], v[90:91], v[26:27] op_sel_hi:[0,1,1]
	v_pk_fma_f32 v[64:65], v[54:55], v[92:93], v[70:71] op_sel_hi:[0,1,1]
	v_pk_fma_f32 v[24:25], v[54:55], v[94:95], v[24:25] op_sel_hi:[0,1,1]
	v_pk_fma_f32 v[66:67], v[54:55], v[96:97], v[72:73] op_sel_hi:[0,1,1]
	v_pk_fma_f32 v[22:23], v[54:55], v[98:99], v[22:23] op_sel_hi:[0,1,1]
	s_waitcnt vmcnt(15)
	v_cvt_pk_f32_fp8_e32 v[54:55], v49
	v_cvt_pk_f32_fp8_sdwa v[68:69], v49 src0_sel:WORD_1
	s_waitcnt vmcnt(14)
	v_cvt_pk_f32_fp8_e32 v[70:71], v132
	v_cvt_pk_f32_fp8_sdwa v[72:73], v132 src0_sel:WORD_1
	s_waitcnt vmcnt(13)
	v_cvt_pk_f32_fp8_e32 v[74:75], v133
	v_cvt_pk_f32_fp8_sdwa v[76:77], v133 src0_sel:WORD_1
	s_waitcnt vmcnt(12)
	v_cvt_pk_f32_fp8_e32 v[78:79], v134
	v_cvt_pk_f32_fp8_sdwa v[80:81], v134 src0_sel:WORD_1
	s_waitcnt vmcnt(11)
	v_cvt_pk_f32_fp8_e32 v[82:83], v135
	v_cvt_pk_f32_fp8_sdwa v[84:85], v135 src0_sel:WORD_1
	s_waitcnt vmcnt(10)
	v_cvt_pk_f32_fp8_e32 v[86:87], v136
	v_cvt_pk_f32_fp8_sdwa v[88:89], v136 src0_sel:WORD_1
	s_waitcnt vmcnt(9)
	v_cvt_pk_f32_fp8_e32 v[90:91], v137
	v_cvt_pk_f32_fp8_sdwa v[92:93], v137 src0_sel:WORD_1
	s_waitcnt vmcnt(8)
	v_cvt_pk_f32_fp8_e32 v[94:95], v138
	v_cvt_pk_f32_fp8_sdwa v[96:97], v138 src0_sel:WORD_1
	s_waitcnt vmcnt(7)
	v_cvt_pk_f32_fp8_e32 v[98:99], v139
	v_cvt_pk_f32_fp8_sdwa v[132:133], v139 src0_sel:WORD_1
	v_pk_fma_f32 v[46:47], v[50:51], v[100:101], v[46:47] op_sel_hi:[0,1,1]
	v_pk_fma_f32 v[36:37], v[50:51], v[102:103], v[36:37] op_sel_hi:[0,1,1]
	s_waitcnt vmcnt(6)
	v_cvt_pk_f32_fp8_e32 v[100:101], v140
	v_cvt_pk_f32_fp8_sdwa v[102:103], v140 src0_sel:WORD_1
	v_pk_fma_f32 v[52:53], v[50:51], v[104:105], v[52:53] op_sel_hi:[0,1,1]
	v_pk_fma_f32 v[34:35], v[50:51], v[106:107], v[34:35] op_sel_hi:[0,1,1]
	s_waitcnt vmcnt(5)
	v_cvt_pk_f32_fp8_e32 v[104:105], v141
	v_cvt_pk_f32_fp8_sdwa v[106:107], v141 src0_sel:WORD_1
	v_pk_fma_f32 v[56:57], v[50:51], v[108:109], v[56:57] op_sel_hi:[0,1,1]
	s_waitcnt vmcnt(4)
	v_cvt_pk_f32_fp8_e32 v[108:109], v142
	v_pk_fma_f32 v[58:59], v[50:51], v[112:113], v[58:59] op_sel_hi:[0,1,1]
	s_waitcnt vmcnt(3)
	v_cvt_pk_f32_fp8_e32 v[112:113], v143
	v_pk_fma_f32 v[60:61], v[50:51], v[116:117], v[60:61] op_sel_hi:[0,1,1]
	s_waitcnt vmcnt(2)
	v_cvt_pk_f32_fp8_e32 v[116:117], v144
	v_pk_fma_f32 v[62:63], v[50:51], v[120:121], v[62:63] op_sel_hi:[0,1,1]
	s_waitcnt vmcnt(1)
	v_cvt_pk_f32_fp8_e32 v[120:121], v145
	v_pk_fma_f32 v[64:65], v[50:51], v[124:125], v[64:65] op_sel_hi:[0,1,1]
	s_waitcnt vmcnt(0)
; __device__ __forceinline__ float wave_sum(float v) {
; #pragma unroll
;     for (int o = 1; o < 64; o <<= 1) v += __shfl_xor(v, o);
;     return v;
; __device__ __forceinline__ void p11_combine(const P& p, int gw, int NGW, int lane, float oscale) {
;     ...
;         float ss = 0.f;
; #pragma unroll
;         for (int j = 0; j < 8; ++j) ss += (a[j].x * a[j].x + a[j].y * a[j].y) + (a[j].z * a[j].z + a[j].w * a[j].w);
;         ss = wave_sum(ss); const float r = rsqrtf(ss * (1.0f / DM) + EPS) * oscale;
	v_cvt_pk_f32_fp8_e32 v[124:125], v146
	v_pk_fma_f32 v[32:33], v[50:51], v[110:111], v[32:33] op_sel_hi:[0,1,1]
	v_cvt_pk_f32_fp8_sdwa v[110:111], v142 src0_sel:WORD_1
	v_pk_fma_f32 v[30:31], v[50:51], v[114:115], v[30:31] op_sel_hi:[0,1,1]
	v_cvt_pk_f32_fp8_sdwa v[114:115], v143 src0_sel:WORD_1
	v_pk_fma_f32 v[28:29], v[50:51], v[118:119], v[28:29] op_sel_hi:[0,1,1]
	v_cvt_pk_f32_fp8_sdwa v[118:119], v144 src0_sel:WORD_1
	v_pk_fma_f32 v[26:27], v[50:51], v[122:123], v[26:27] op_sel_hi:[0,1,1]
	v_cvt_pk_f32_fp8_sdwa v[122:123], v145 src0_sel:WORD_1
	v_pk_fma_f32 v[24:25], v[50:51], v[126:127], v[24:25] op_sel_hi:[0,1,1]
	v_cvt_pk_f32_fp8_sdwa v[126:127], v146 src0_sel:WORD_1
	v_pk_fma_f32 v[66:67], v[50:51], v[128:129], v[66:67] op_sel_hi:[0,1,1]
	v_pk_fma_f32 v[22:23], v[50:51], v[130:131], v[22:23] op_sel_hi:[0,1,1]
	v_pk_fma_f32 v[46:47], v[50:51], v[54:55], v[46:47] op_sel:[1,0,0]
	v_pk_fma_f32 v[36:37], v[50:51], v[68:69], v[36:37] op_sel:[1,0,0]
	v_pk_fma_f32 v[52:53], v[50:51], v[70:71], v[52:53] op_sel:[1,0,0]
	v_pk_fma_f32 v[34:35], v[50:51], v[72:73], v[34:35] op_sel:[1,0,0]
	v_pk_fma_f32 v[54:55], v[50:51], v[74:75], v[56:57] op_sel:[1,0,0]
	v_pk_fma_f32 v[32:33], v[50:51], v[76:77], v[32:33] op_sel:[1,0,0]
	v_pk_fma_f32 v[56:57], v[50:51], v[78:79], v[58:59] op_sel:[1,0,0]
	v_pk_fma_f32 v[30:31], v[50:51], v[80:81], v[30:31] op_sel:[1,0,0]
	v_pk_fma_f32 v[58:59], v[50:51], v[82:83], v[60:61] op_sel:[1,0,0]
	v_pk_fma_f32 v[28:29], v[50:51], v[84:85], v[28:29] op_sel:[1,0,0]
	v_pk_fma_f32 v[60:61], v[50:51], v[86:87], v[62:63] op_sel:[1,0,0]
	v_pk_fma_f32 v[26:27], v[50:51], v[88:89], v[26:27] op_sel:[1,0,0]
	v_pk_fma_f32 v[62:63], v[50:51], v[90:91], v[64:65] op_sel:[1,0,0]
	v_pk_fma_f32 v[24:25], v[50:51], v[92:93], v[24:25] op_sel:[1,0,0]
	v_pk_fma_f32 v[64:65], v[50:51], v[94:95], v[66:67] op_sel:[1,0,0]
	v_pk_fma_f32 v[22:23], v[50:51], v[96:97], v[22:23] op_sel:[1,0,0]
	v_pk_fma_f32 v[46:47], v[48:49], v[98:99], v[46:47] op_sel_hi:[0,1,1]
	v_pk_fma_f32 v[36:37], v[48:49], v[132:133], v[36:37] op_sel_hi:[0,1,1]
	v_pk_fma_f32 v[50:51], v[48:49], v[100:101], v[52:53] op_sel_hi:[0,1,1]
	v_pk_fma_f32 v[34:35], v[48:49], v[102:103], v[34:35] op_sel_hi:[0,1,1]
	v_pk_fma_f32 v[52:53], v[48:49], v[104:105], v[54:55] op_sel_hi:[0,1,1]
	v_pk_fma_f32 v[32:33], v[48:49], v[106:107], v[32:33] op_sel_hi:[0,1,1]
	v_pk_fma_f32 v[54:55], v[48:49], v[108:109], v[56:57] op_sel_hi:[0,1,1]
	v_pk_fma_f32 v[56:57], v[48:49], v[112:113], v[58:59] op_sel_hi:[0,1,1]
	v_pk_fma_f32 v[58:59], v[48:49], v[116:117], v[60:61] op_sel_hi:[0,1,1]
	v_pk_fma_f32 v[60:61], v[48:49], v[120:121], v[62:63] op_sel_hi:[0,1,1]
	v_pk_fma_f32 v[62:63], v[48:49], v[124:125], v[64:65] op_sel_hi:[0,1,1]
	v_mov_b32_e32 v64, v47
	v_mov_b32_e32 v65, v51
	v_mov_b32_e32 v68, v37
	v_mov_b32_e32 v69, v35
	v_pk_fma_f32 v[30:31], v[48:49], v[110:111], v[30:31] op_sel_hi:[0,1,1]
	v_pk_fma_f32 v[28:29], v[48:49], v[114:115], v[28:29] op_sel_hi:[0,1,1]
	v_pk_fma_f32 v[26:27], v[48:49], v[118:119], v[26:27] op_sel_hi:[0,1,1]
	v_pk_fma_f32 v[24:25], v[48:49], v[122:123], v[24:25] op_sel_hi:[0,1,1]
	v_pk_fma_f32 v[22:23], v[48:49], v[126:127], v[22:23] op_sel_hi:[0,1,1]
	v_mov_b32_e32 v48, v46
	v_mov_b32_e32 v49, v50
	v_mov_b32_e32 v66, v36
	v_mov_b32_e32 v67, v34
	v_mov_b32_e32 v72, v53
	v_mov_b32_e32 v73, v33
	v_pk_mul_f32 v[64:65], v[64:65], v[64:65]
	v_pk_mul_f32 v[68:69], v[68:69], v[68:69]
	v_mov_b32_e32 v70, v52
	v_mov_b32_e32 v71, v32
	v_pk_mul_f32 v[72:73], v[72:73], v[72:73]
	v_pk_fma_f32 v[48:49], v[48:49], v[48:49], v[64:65]
	v_pk_fma_f32 v[64:65], v[66:67], v[66:67], v[68:69]
	v_mul_f32_e32 v74, v55, v55
	v_mul_f32_e32 v76, v31, v31
	v_pk_fma_f32 v[66:67], v[70:71], v[70:71], v[72:73]
	v_pk_add_f32 v[48:49], v[48:49], v[64:65]
	v_pk_mul_f32 v[78:79], v[56:57], v[56:57]
	v_pk_mul_f32 v[80:81], v[28:29], v[28:29]
	v_pk_fma_f32 v[74:75], v[54:55], v[54:55], v[74:75] op_sel_hi:[1,1,0]
	v_pk_fma_f32 v[76:77], v[30:31], v[30:31], v[76:77] op_sel_hi:[1,1,0]
	v_pk_add_f32 v[64:65], v[66:67], v[66:67] op_sel:[0,1] op_sel_hi:[1,0]
	v_pk_add_f32 v[48:49], v[48:49], v[48:49] op_sel:[0,1] op_sel_hi:[1,0]
	v_mov_b32_e32 v84, v59
	v_mov_b32_e32 v85, v27
	v_mov_b32_e32 v75, v80
	v_mov_b32_e32 v77, v81
	v_mov_b32_e32 v65, v79
	v_mov_b32_e32 v49, v78
	v_mov_b32_e32 v82, v58
	v_mov_b32_e32 v83, v26
	v_pk_mul_f32 v[84:85], v[84:85], v[84:85]
	v_pk_add_f32 v[66:67], v[74:75], v[76:77]
	v_pk_add_f32 v[48:49], v[48:49], v[64:65]
	v_mul_f32_e32 v86, v61, v61
	v_mul_f32_e32 v88, v25, v25
	v_pk_fma_f32 v[68:69], v[82:83], v[82:83], v[84:85]
	v_pk_add_f32 v[48:49], v[48:49], v[66:67]
	v_pk_mul_f32 v[90:91], v[62:63], v[62:63]
	v_pk_mul_f32 v[92:93], v[22:23], v[22:23]
	v_pk_fma_f32 v[86:87], v[60:61], v[60:61], v[86:87] op_sel_hi:[1,1,0]
	v_pk_fma_f32 v[88:89], v[24:25], v[24:25], v[88:89] op_sel_hi:[1,1,0]
	v_pk_add_f32 v[68:69], v[68:69], v[68:69] op_sel:[0,1] op_sel_hi:[1,0]
	v_pk_add_f32 v[48:49], v[48:49], v[48:49] op_sel:[0,1] op_sel_hi:[1,0]
	v_mov_b32_e32 v87, v92
	v_mov_b32_e32 v89, v93
	v_mov_b32_e32 v69, v91
	v_mov_b32_e32 v49, v90
	v_pk_add_f32 v[70:71], v[86:87], v[88:89]
	v_pk_add_f32 v[48:49], v[48:49], v[68:69]
	s_nop 0
	v_pk_add_f32 v[48:49], v[48:49], v[70:71]
	s_nop 0
	v_add_f32_e32 v48, v48, v49
	ds_bpermute_b32 v49, v40, v48
	s_waitcnt lgkmcnt(0)
; #define GAS __attribute__((address_space(1)))
; __device__ __forceinline__ float wave_sum(float v) {
; #pragma unroll
;     for (int o = 1; o < 64; o <<= 1) v += __shfl_xor(v, o);
;     return v;
; __device__ __forceinline__ void p11_combine(const P& p, int gw, int NGW, int lane, float oscale) {
;     ...
;         ss = wave_sum(ss); const float r = rsqrtf(ss * (1.0f / DM) + EPS) * oscale;
;         const GAS f32x4* gf = (const GAS f32x4*)p.g_fin + lane;
; #pragma unroll
;         for (int j = 0; j < 8; ++j) { const f32x4 g = gf[64 * j]; xr[64 * j] = a[j] * r * g; }
	v_add_f32_e32 v48, v48, v49
	ds_bpermute_b32 v49, v41, v48
	s_waitcnt lgkmcnt(0)
	v_add_f32_e32 v48, v48, v49
	ds_bpermute_b32 v49, v42, v48
	s_waitcnt lgkmcnt(0)
	v_add_f32_e32 v48, v48, v49
	ds_bpermute_b32 v49, v43, v48
	s_waitcnt lgkmcnt(0)
	v_add_f32_e32 v48, v48, v49
	ds_bpermute_b32 v49, v44, v48
	s_waitcnt lgkmcnt(0)
	v_add_f32_e32 v48, v48, v49
	ds_bpermute_b32 v49, v45, v48
	s_waitcnt lgkmcnt(0)
	v_add_f32_e32 v48, v48, v49
	v_fmamk_f32 v48, v48, 0x3a000000, v4
	v_mul_f32_e32 v49, 0x4b800000, v48
	v_cmp_gt_f32_e32 vcc, s13, v48
	s_nop 1
	v_cndmask_b32_e32 v48, v48, v49, vcc
	v_rsq_f32_e32 v48, v48
	s_nop 0
	v_mul_f32_e32 v49, 0x45800000, v48
	v_cndmask_b32_e32 v48, v48, v49, vcc
	v_pk_mul_f32 v[46:47], v[46:47], v[48:49] op_sel_hi:[1,0]
	v_pk_mul_f32 v[36:37], v[36:37], v[48:49] op_sel_hi:[1,0]
	v_pk_mul_f32 v[0:1], v[0:1], v[46:47]
	v_pk_mul_f32 v[2:3], v[2:3], v[36:37]
	global_store_dwordx4 v[18:19], v[0:3], off offset:-4096
	v_pk_mul_f32 v[34:35], v[34:35], v[48:49] op_sel_hi:[1,0]
	v_pk_mul_f32 v[36:37], v[50:51], v[48:49] op_sel_hi:[1,0]
	v_pk_mul_f32 v[32:33], v[32:33], v[48:49] op_sel_hi:[1,0]
	v_pk_mul_f32 v[30:31], v[30:31], v[48:49] op_sel_hi:[1,0]
	v_pk_mul_f32 v[28:29], v[28:29], v[48:49] op_sel_hi:[1,0]
	v_pk_mul_f32 v[26:27], v[26:27], v[48:49] op_sel_hi:[1,0]
	v_pk_mul_f32 v[24:25], v[24:25], v[48:49] op_sel_hi:[1,0]
	v_pk_mul_f32 v[22:23], v[22:23], v[48:49] op_sel_hi:[1,0]
	v_pk_mul_f32 v[192:193], v[164:165], v[36:37]
	v_pk_mul_f32 v[194:195], v[166:167], v[34:35]
	global_store_dwordx4 v[18:19], v[192:195], off offset:-3072
	v_pk_mul_f32 v[34:35], v[52:53], v[48:49] op_sel_hi:[1,0]
	v_pk_mul_f32 v[2:3], v[170:171], v[32:33]
	v_pk_mul_f32 v[0:1], v[168:169], v[34:35]
	global_store_dwordx4 v[18:19], v[0:3], off offset:-2048
	v_pk_mul_f32 v[32:33], v[54:55], v[48:49] op_sel_hi:[1,0]
	v_pk_mul_f32 v[194:195], v[174:175], v[30:31]
	v_pk_mul_f32 v[192:193], v[172:173], v[32:33]
	global_store_dwordx4 v[18:19], v[192:195], off offset:-1024
	v_pk_mul_f32 v[30:31], v[56:57], v[48:49] op_sel_hi:[1,0]
	v_pk_mul_f32 v[2:3], v[178:179], v[28:29]
	v_pk_mul_f32 v[0:1], v[176:177], v[30:31]
	global_store_dwordx4 v[18:19], v[0:3], off
	v_pk_mul_f32 v[28:29], v[58:59], v[48:49] op_sel_hi:[1,0]
	v_pk_mul_f32 v[194:195], v[182:183], v[26:27]
	v_pk_mul_f32 v[192:193], v[180:181], v[28:29]
	global_store_dwordx4 v[18:19], v[192:195], off offset:1024
	v_pk_mul_f32 v[26:27], v[60:61], v[48:49] op_sel_hi:[1,0]
	v_pk_mul_f32 v[2:3], v[186:187], v[24:25]
	v_pk_mul_f32 v[0:1], v[184:185], v[26:27]
	global_store_dwordx4 v[18:19], v[0:3], off offset:2048
	v_pk_mul_f32 v[24:25], v[62:63], v[48:49] op_sel_hi:[1,0]
	v_pk_mul_f32 v[194:195], v[190:191], v[22:23]
	v_pk_mul_f32 v[192:193], v[188:189], v[24:25]
	global_store_dwordx4 v[18:19], v[192:195], off offset:3072
	v_lshl_add_u64 v[18:19], v[18:19], 0, s[2:3]
	s_cbranch_scc1 .LBB5_1742
